# speedup vs baseline: 1.0090x; 1.0090x over previous
.Lc0_fin2:
	ds_read_b128 v[112:115], v43 offset:2048
	ds_read_b128 v[116:119], v43 offset:3072
	s_waitcnt lgkmcnt(0)
	v_pk_add_f16 v112, v112, v116
	v_pk_add_f16 v113, v113, v117
	v_pk_add_f16 v114, v114, v118
	v_pk_add_f16 v115, v115, v119
	s_mov_b32 exec_lo, -1
	s_mov_b32 exec_hi, 0
	global_store_dwordx4 v35, v[112:115], s[68:69]
